# nt cache policy also on the T3a chunk input loads (keeps the item records written in T3a in cache for T3b)
# baseline (speedup 1.0000x reference)
; __device__ __forceinline__ int lane_id() { int l; asm volatile("v_mbcnt_lo_u32_b32 %0, -1, 0\n\tv_mbcnt_hi_u32_b32 %0, -1, %0" : "=v"(l)); return l; }
; #define P1_PIN(v) asm volatile("" : "+v"(v.x), "+v"(v.y), "+v"(v.z), "+v"(v.w))
; __device__ __forceinline__ void phase1(const int WID_, const In& I, char* lds) {
;     ...
;     { const int t0 = wv * 64 + lane_id();
;       for (int i = t0; i < 1536; i += NT) CST[i] = (_Float16)I.mu[i];
;       CST[1536 + t0] = (_Float16)I.k_k[t0]; CST[2048 + t0] = (_Float16)I.k_a[t0]; CST[2560 + t0] = (_Float16)I.r_k[t0]; }
;     __syncthreads();
;     uint4 nx_r, nx_k, nx_v, nx_qr, nx_qk, nx_qv, nx_a, nx_l;
;     ...
;     P1_LOADS(GB);
;     P1_PIN(nx_r); P1_PIN(nx_k); P1_PIN(nx_v); P1_PIN(nx_qr); P1_PIN(nx_qk); P1_PIN(nx_qv); P1_PIN(nx_a); P1_PIN(nx_l);
;     for (int item = GB; item < NB * 8 * (S / 64); item += GN) {
.LBB0_1411:
	s_or_b64 exec, exec, s[0:1]
	v_ashrrev_i32_e32 v1, 31, v0
	v_readlane_b32 s36, v243, 6
	v_lshlrev_b64 v[2:3], 2, v[0:1]
	v_readlane_b32 s40, v243, 10
	v_readlane_b32 s41, v243, 11
	v_readlane_b32 s42, v243, 12
	v_readlane_b32 s43, v243, 13
	v_lshl_add_u64 v[4:5], s[40:41], 0, v[2:3]
	v_readlane_b32 s44, v243, 14
	v_readlane_b32 s45, v243, 15
	global_load_dword v1, v[4:5], off
	v_lshl_add_u64 v[4:5], s[42:43], 0, v[2:3]
	global_load_dword v4, v[4:5], off
	v_lshl_add_u64 v[2:3], s[44:45], 0, v[2:3]
	global_load_dword v5, v[2:3], off
	s_add_u32 s4, s92, 0x30000000
	s_addc_u32 s5, s93, 0
	s_add_u32 s10, s92, 0x22000000
	s_addc_u32 s11, s93, 0
	s_add_i32 s0, 0, 0x21c00
	s_min_i32 s1, s87, 0x1fff
	v_lshl_add_u32 v0, v0, 1, s0
	s_ashr_i32 s0, s1, 10
	s_lshr_b32 s2, s1, 1
	s_lshl_b32 s1, s1, 6
	s_and_b32 s2, s2, 0x1c0
	s_and_b32 s3, s1, 0x1fc0
	s_ashr_i32 s1, s0, 31
	s_lshl_b64 s[0:1], s[0:1], 13
	s_movk_i32 s8, 0xe00
	v_mov_b64_e32 v[2:3], s[92:93]
	v_mov_b32_e32 v69, 0
	v_mov_b32_e32 v76, 0xfffff200
	v_writelane_b32 v242, s4, 37
	s_cmpk_gt_i32 s87, 0x1fff
	v_readlane_b32 s37, v243, 7
	v_writelane_b32 v242, s5, 38
	v_readlane_b32 s38, v243, 8
	v_readlane_b32 s39, v243, 9
	v_readlane_b32 s46, v243, 16
	v_readlane_b32 s47, v243, 17
	v_readlane_b32 s48, v243, 18
	v_readlane_b32 s49, v243, 19
	v_readlane_b32 s50, v243, 20
	v_readlane_b32 s51, v243, 21
	s_waitcnt vmcnt(2)
	v_cvt_f16_f32_e32 v1, v1
	s_waitcnt vmcnt(1)
	v_cvt_f16_f32_e32 v4, v4
	s_waitcnt vmcnt(0)
	v_cvt_f16_f32_e32 v5, v5
	ds_write_b16 v0, v1 offset:3072
	ds_write_b16 v0, v4 offset:4096
	ds_write_b16 v0, v5 offset:5120
	s_waitcnt lgkmcnt(0)
	s_barrier
	v_mbcnt_lo_u32_b32 v0, -1, 0
	v_mbcnt_hi_u32_b32 v0, -1, v0
	s_nop 0
	v_add_u32_e32 v1, s86, v0
	v_lshlrev_b32_e32 v0, 3, v0
	v_ashrrev_i32_e32 v1, 3, v1
	v_and_or_b32 v4, v0, 56, s2
	v_add_u32_e32 v0, s3, v1
	v_ashrrev_i32_e32 v1, 31, v0
	v_lshlrev_b32_e32 v68, 1, v4
	v_lshl_add_u64 v[4:5], s[0:1], 0, v[0:1]
	v_mad_u64_u32 v[2:3], s[0:1], v4, s8, v[2:3]
	v_lshlrev_b64 v[6:7], 10, v[4:5]
	v_mad_i32_i24 v3, v5, s8, v3
	v_lshl_add_u64 v[4:5], s[4:5], 0, v[6:7]
	v_lshl_add_u64 v[6:7], s[28:29], 0, v[6:7]
	v_lshl_add_u64 v[2:3], v[2:3], 0, v[68:69]
	v_cmp_lt_i32_e32 vcc, 0, v0
	v_lshl_add_u64 v[4:5], v[4:5], 0, v[68:69]
	global_load_dwordx4 v[36:39], v[2:3], off nt
	v_lshl_add_u64 v[6:7], v[6:7], 0, v[68:69]
	global_load_dwordx4 v[28:31], v[2:3], off offset:1024 nt
	global_load_dwordx4 v[32:35], v[4:5], off nt
	global_load_dwordx4 v[40:43], v[6:7], off nt
	v_cndmask_b32_e64 v1, 0, -1, vcc
	v_cndmask_b32_e32 v0, 0, v76, vcc
	v_lshl_add_u64 v[0:1], v[2:3], 0, v[0:1]
	global_load_dwordx4 v[20:23], v[2:3], off offset:2048 nt
	global_load_dwordx4 v[44:47], v[0:1], off nt
	global_load_dwordx4 v[24:27], v[0:1], off offset:2048 nt
	global_load_dwordx4 v[48:51], v[0:1], off offset:1024 nt
	s_mov_b32 s5, 0
	s_waitcnt vmcnt(6)
	v_mov_b32_e32 v3, v29
	v_mov_b32_e32 v6, v36
	v_mov_b32_e32 v7, v37
	v_mov_b32_e32 v5, v28
	s_waitcnt vmcnt(5)
	v_mov_b32_e32 v0, v33
	s_waitcnt vmcnt(4)
	v_mov_b32_e32 v8, v43
	v_mov_b32_e32 v9, v42
	s_waitcnt vmcnt(2)
	v_mov_b32_e32 v4, v45
	s_waitcnt vmcnt(1)
	v_mov_b32_e32 v1, v24
	v_mov_b32_e32 v2, v25
	s_waitcnt vmcnt(0)
	s_cbranch_scc1 .LBB0_1473
	v_readlane_b32 s7, v243, 42
	s_cmpk_lt_u32 s7, 0x300
	v_readlane_b32 s6, v243, 44
	s_cselect_b64 s[2:3], -1, 0
	s_cmp_lg_u32 s6, 1
	s_cselect_b64 s[14:15], -1, 0
	s_cmpk_gt_u32 s7, 0xff
	s_cselect_b64 s[16:17], -1, 0
	s_lshl_b32 s0, s6, 4
	s_and_b32 s0, s0, 0x3fffffe0
	s_mul_i32 s1, s0, 0x90
	s_lshl_b32 s35, s6, 5
	s_add_i32 s34, s1, 0
	s_and_b32 s1, s35, 32
	s_mulk_i32 s1, 0x90
	s_add_i32 s47, s1, 0
	s_lshl_b32 s0, s0, 1
	s_add_i32 s34, s34, 0x14400
	s_add_i32 s46, s47, 0x12000
	s_add_i32 s47, s47, s0
	s_cmpk_lt_u32 s7, 0x80
	s_cselect_b64 s[18:19], -1, 0
	s_lshl_b32 s0, s6, 6
	s_add_i32 s48, s0, 0
	s_mul_i32 s0, s6, 0xa00
	s_add_i32 s50, s0, 0
	s_mul_i32 s0, s6, 0x300
	s_add_i32 s51, s0, 0
	s_lshl_b32 s0, s6, 3
	s_and_b32 s0, s0, 0x1fffffe0
	s_mul_i32 s1, s0, 0x90
	s_add_i32 s53, s1, 0
	s_and_b32 s1, s35, 0x60
	s_mulk_i32 s1, 0x90
	s_add_i32 s58, s1, 0
	s_lshl_b32 s0, s0, 1
	s_add_i32 s59, s58, s0
	s_bfe_u32 s0, s7, 0x10007
	s_lshl_b32 s4, s0, 6
	s_bfe_u32 s1, s7, 0x10006
	s_add_i32 s66, s4, 0
	s_mul_i32 s4, s0, 0x11c0
	s_add_i32 s67, s66, s4
	s_mul_i32 s4, s1, 0x900
	s_lshl_b32 s60, s0, 5
	s_mul_i32 s61, s0, 0x1200
	s_lshl_b32 s62, s1, 5
	s_mul_i32 s63, s1, 0x1200
	s_lshl_b32 s68, s4, 1
	s_lshl_b32 s0, s0, 9
	s_lshl_b32 s1, s1, 7
	s_add_i32 s49, s48, 0x14d00
	s_add_i32 s50, s50, 0x1f400
	s_add_i32 s51, s51, 0x20800
	s_or_b32 s52, s35, 16
	s_add_i32 s69, s68, 0
	s_or_b32 s70, s1, s0
	s_cmpk_gt_u32 s7, 0x1ff
	s_cselect_b64 s[20:21], -1, 0
	s_and_b32 s0, s7, 0xffffff00
	s_cmpk_lg_i32 s0, 0x200
	s_cselect_b64 s[22:23], -1, 0
	s_cmpk_lt_u32 s7, 0x100
	s_mov_b32 s0, 0xd800
	s_cselect_b32 s71, s0, 0x18c00
	s_mov_b32 s0, 0xfc00
	s_cselect_b32 s76, s0, 0x1b000
	s_movk_i32 s0, 0x4000
	s_cselect_b32 s36, s0, 0x6000
	s_add_i32 s0, s6, 8
	s_and_b32 s0, s0, 0x7fffffc
	s_cmp_lg_u32 s0, 8
	s_movk_i32 s9, 0x90
	s_mov_b32 s37, s5
	s_cselect_b64 s[38:39], -1, 0
	s_add_i32 s77, 0, 0x1d400
	v_mov_b32_e32 v77, 0x260
	s_add_i32 s78, 0, 0x15600
	v_mov_b32_e32 v16, v69
	v_mov_b32_e32 v17, v69
	v_mov_b32_e32 v18, v69
	v_mov_b32_e32 v19, v69
	s_mov_b32 s40, s87
	v_mov_b32_e32 v42, v9
	v_mov_b32_e32 v43, v8
	v_mov_b32_e32 v36, v6
	v_mov_b32_e32 v37, v7
	v_mov_b32_e32 v28, v5
	v_mov_b32_e32 v29, v3
	v_mov_b32_e32 v45, v4
	v_mov_b32_e32 v24, v1
	v_mov_b32_e32 v25, v2
	v_mov_b32_e32 v33, v0
	s_branch .LBB0_1414

; __device__ __forceinline__ void phase1(const int WID_, const In& I, char* lds) {
;     ...
;             for (int e = 0; e < 8; ++e) { const int w_ = e >> 1; const bool hi = e & 1;
;                 auto ex = [&](unsigned u) { return hi ? __builtin_bit_cast(float, u & 0xffff0000u) : __builtin_bit_cast(float, u << 16); };
;                 float x = ex(wr[w_]); r_[e] = x + (ex(pr[w_]) - x) * mur[e];
;                 x = ex(wk[w_]); const float k = x + (ex(pk[w_]) - x) * muk[e];
;                 x = ex(wv4[w_]); v_[e] = x + (ex(pv[w_]) - x) * muv[e];
;                 a_[e] = ex(wa[w_]); kk_[e] = k * ckk[e]; ss += kk_[e] * kk_[e];
;                 kp_[e] = k * (1.f + (a_[e] - 1.f) * cka[e]); rk += r_[e] * kp_[e] * crk[e];
;                 G[s * 64 + cg * 8 + e] = ex(wl[w_]); }
;             ss += dpp16<0xB1>(ss); ss += dpp16<0x4E>(ss); ss += dpp16<0x141>(ss);
;             const float inv = 1.f / fmaxf(sqrtf(ss), 1e-12f);
; #pragma unroll
;             for (int e = 0; e < 8; ++e) { kk_[e] *= inv; b_[e] = kk_[e] * a_[e]; }
;             rk += dpp16<0xB1>(rk); rk += dpp16<0x4E>(rk); rk += dpp16<0x141>(rk);
;             if (cg == 0) I.RK[m * 8 + h] = rk;
;         }
;         CK_BAR();
;         { const int ch = tid & 63, part = tid >> 6; float run = 0.f;
; #pragma unroll
;           for (int i = 0; i < 8; ++i) { run += G[(8 * part + i) * 64 + ch]; G[(8 * part + i) * 64 + ch] = run; }
;           TOT[part * 64 + ch] = run; }
;         CK_BAR();
;         { const int ch = tid & 63, part = tid >> 6; float off = 0.f;
;           for (int p = 0; p < part; ++p) off += TOT[p * 64 + ch];
; #pragma unroll
;           for (int i = 0; i < 8; ++i) G[(8 * part + i) * 64 + ch] += off; }
;         CK_BAR();
;         float glast[8];
;         {
;             unsigned pab[4], prb[4], pbb[4], pkb[4];
;             float ab[8], rb[8], bb[8], kb[8], bt[8], kt[8];
;             const float4 g0_ = *(const float4*)(G + s * 64 + cg * 8), g1_ = *(const float4*)(G + s * 64 + cg * 8 + 4);
;             const int sm = (s > 0) ? s - 1 : 0; const float msk = (s > 0) ? 1.f : 0.f;
;             const float4 m0_ = *(const float4*)(G + sm * 64 + cg * 8), m1_ = *(const float4*)(G + sm * 64 + cg * 8 + 4);
;             const float4 l0_ = *(const float4*)(G + 63 * 64 + cg * 8), l1_ = *(const float4*)(G + 63 * 64 + cg * 8 + 4);
.Lscan_done:
	s_waitcnt lgkmcnt(0)
	v_cndmask_b32_e32 v6, 0, v24, vcc
	v_cndmask_b32_e32 v7, 0, v26, vcc
	v_cndmask_b32_e32 v24, 0, v25, vcc
	v_cndmask_b32_e32 v25, 0, v27, vcc
	v_lshlrev_b32_e32 v26, 16, v20
	v_lshlrev_b32_e32 v27, 16, v6
	v_and_b32_e32 v20, 0xffff0000, v20
	v_and_b32_e32 v6, 0xffff0000, v6
	v_sub_f32_e32 v27, v27, v26
	v_sub_f32_e32 v6, v6, v20
	v_fma_mix_f32 v53, v27, v0, v26 op_sel_hi:[0,1,0]
	v_fma_mix_f32 v68, v6, v0, v20 op_sel:[0,1,0] op_sel_hi:[0,1,0]
	v_lshlrev_b32_e32 v0, 16, v21
	v_lshlrev_b32_e32 v6, 16, v24
	v_sub_f32_e32 v6, v6, v0
	v_fma_mix_f32 v72, v6, v1, v0 op_sel_hi:[0,1,0]
	v_and_b32_e32 v0, 0xffff0000, v21
	v_and_b32_e32 v6, 0xffff0000, v24
	v_sub_f32_e32 v6, v6, v0
	v_fma_mix_f32 v73, v6, v1, v0 op_sel:[0,1,0] op_sel_hi:[0,1,0]
	v_lshlrev_b32_e32 v0, 16, v22
	v_lshlrev_b32_e32 v1, 16, v7
	v_sub_f32_e32 v1, v1, v0
	v_fma_mix_f32 v74, v1, v2, v0 op_sel_hi:[0,1,0]
	v_and_b32_e32 v0, 0xffff0000, v22
	v_and_b32_e32 v1, 0xffff0000, v7
	v_sub_f32_e32 v1, v1, v0
	v_fma_mix_f32 v75, v1, v2, v0 op_sel:[0,1,0] op_sel_hi:[0,1,0]
	v_add_f32_e32 v2, v56, v57
	s_mov_b32 s0, 0xf800000
	v_mul_f32_e32 v6, 0x4f800000, v2
	v_cmp_gt_f32_e32 vcc, s0, v2
	v_lshlrev_b32_e32 v0, 16, v23
	v_lshlrev_b32_e32 v1, 16, v25
	v_cndmask_b32_e32 v2, v2, v6, vcc
	v_sqrt_f32_e32 v6, v2
	v_sub_f32_e32 v1, v1, v0
	v_fma_mix_f32 v78, v1, v3, v0 op_sel_hi:[0,1,0]
	v_and_b32_e32 v0, 0xffff0000, v23
	v_add_u32_e32 v1, -1, v6
	v_fma_f32 v7, -v1, v6, v2
	v_cmp_ge_f32_e64 s[0:1], 0, v7
	v_add_u32_e32 v7, 1, v6
	v_lshlrev_b32_e32 v52, 3, v61
	v_cndmask_b32_e64 v1, v6, v1, s[0:1]
	v_fma_f32 v6, -v7, v6, v2
	v_cmp_lt_f32_e64 s[0:1], 0, v6
	s_add_i32 s33, s40, s94
	s_nop 0
	v_cndmask_b32_e64 v1, v1, v7, s[0:1]
	v_mul_f32_e32 v6, 0x37800000, v1
	v_cndmask_b32_e32 v1, v1, v6, vcc
	v_cmp_class_f32_e32 vcc, v2, v77
	v_and_b32_e32 v7, 0xffff0000, v25
	v_sub_f32_e32 v7, v7, v0
	v_cndmask_b32_e32 v1, v1, v2, vcc
	v_max_f32_e32 v1, 0x2b8cbccc, v1
	v_div_scale_f32 v2, s[0:1], v1, v1, 1.0
	v_rcp_f32_e32 v6, v2
	v_fma_mix_f32 v79, v7, v3, v0 op_sel:[0,1,0] op_sel_hi:[0,1,0]
	s_movk_i32 s0, 0xff00
	s_min_i32 s1, s33, 0x1fff
	v_fma_f32 v0, -v2, v6, 1.0
	v_fmac_f32_e32 v6, v0, v6
	v_div_scale_f32 v0, vcc, 1.0, v1, 1.0
	v_mul_f32_e32 v3, v0, v6
	v_fma_f32 v7, -v2, v3, v0
	v_fmac_f32_e32 v3, v7, v6
	v_fma_f32 v0, -v2, v3, v0
	v_div_fmas_f32 v0, v0, v6, v3
	v_div_fixup_f32 v0, v0, v1, 1.0
	v_pk_mul_f32 v[54:55], v[8:9], v[0:1] op_sel_hi:[1,0]
	v_pk_mul_f32 v[50:51], v[50:51], v[0:1] op_sel_hi:[1,0]
	v_pk_mul_f32 v[66:67], v[10:11], v[0:1] op_sel_hi:[1,0]
	v_pk_mul_f32 v[48:49], v[48:49], v[0:1] op_sel_hi:[1,0]
	ds_read2st64_b32 v[0:1], v4 offset1:1
	ds_read2st64_b32 v[2:3], v4 offset0:2 offset1:3
	ds_read2st64_b32 v[6:7], v4 offset0:4 offset1:5
	ds_read2st64_b32 v[8:9], v4 offset0:6 offset1:7
	v_pk_mul_f32 v[56:57], v[54:55], v[44:45]
	v_pk_mul_f32 v[64:65], v[50:51], v[42:43]
	v_cmp_lt_i32_e32 vcc, 0, v60
	s_waitcnt lgkmcnt(3)
	v_add_f32_e32 v0, v5, v0
	v_add_f32_e32 v1, v5, v1
	ds_write2st64_b32 v4, v0, v1 offset1:1
	s_waitcnt lgkmcnt(3)
	v_add_f32_e32 v0, v5, v2
	v_add_f32_e32 v1, v5, v3
	ds_write2st64_b32 v4, v0, v1 offset0:2 offset1:3
	s_waitcnt lgkmcnt(3)
	v_add_f32_e32 v0, v5, v6
	v_add_f32_e32 v1, v5, v7
	ds_write2st64_b32 v4, v0, v1 offset0:4 offset1:5
	s_waitcnt lgkmcnt(3)
	v_add_f32_e32 v0, v5, v8
	v_add_f32_e32 v1, v5, v9
	ds_write2st64_b32 v4, v0, v1 offset0:6 offset1:7
	v_max_i32_e32 v0, 1, v60
	v_lshl_add_u32 v0, v0, 8, s77
	v_lshlrev_b32_e32 v1, 2, v52
	s_waitcnt lgkmcnt(0)
	s_barrier
	v_add3_u32 v0, v0, v1, s0
	ds_read_b128 v[8:11], v62
	ds_read_b128 v[20:23], v62 offset:16
	ds_read_b128 v[24:27], v0
	ds_read_b128 v[42:45], v0 offset:16
	v_add_u32_e32 v0, 0, v1
	v_add_u32_e32 v0, 0x21300, v0
	ds_read_b128 v[4:7], v0
	ds_read_b128 v[0:3], v0 offset:16
	v_cndmask_b32_e64 v80, 0, 1.0, vcc
	s_waitcnt lgkmcnt(3)
	v_mul_f32_e32 v63, v80, v24
	v_mul_f32_e32 v24, 0x3fb8aa3b, v8
	v_mul_f32_e32 v62, 0xbfb8aa3b, v8
	s_waitcnt lgkmcnt(1)
	v_sub_f32_e32 v8, v4, v8
	v_mul_f32_e32 v8, 0x3fb8aa3b, v8
	v_exp_f32_e32 v8, v8
	v_mul_f32_e32 v63, 0x3fb8aa3b, v63
	v_exp_f32_e32 v70, v63
	v_mul_f32_e32 v63, 0xbfb8aa3b, v9
	v_mul_f32_e32 v81, v56, v8
	v_mul_f32_e32 v82, v14, v8
	v_mul_f32_e32 v8, v80, v25
	v_mul_f32_e32 v8, 0x3fb8aa3b, v8
	v_exp_f32_e32 v71, v8
	v_sub_f32_e32 v8, v5, v9
	v_mul_f32_e32 v25, 0x3fb8aa3b, v9
	v_mul_f32_e32 v8, 0x3fb8aa3b, v8
	v_exp_f32_e32 v24, v24
	v_exp_f32_e32 v62, v62
	v_exp_f32_e32 v25, v25
	v_exp_f32_e32 v63, v63
	v_exp_f32_e32 v8, v8
	v_mul_f32_e32 v9, v80, v26
	v_pk_mul_f32 v[12:13], v[12:13], v[24:25]
	v_pk_mul_f32 v[24:25], v[56:57], v[62:63]
	v_pk_mul_f32 v[62:63], v[14:15], v[62:63]
	v_mul_f32_e32 v56, v57, v8
	v_mul_f32_e32 v57, v15, v8
	v_mul_f32_e32 v8, 0x3fb8aa3b, v10
	v_mul_f32_e32 v14, 0xbfb8aa3b, v10
	v_sub_f32_e32 v10, v6, v10
	v_mul_f32_e32 v10, 0x3fb8aa3b, v10
	v_exp_f32_e32 v10, v10
	v_pk_mul_f32 v[54:55], v[70:71], v[54:55] neg_lo:[0,1] neg_hi:[0,1]
	v_mul_f32_e32 v9, 0x3fb8aa3b, v9
	v_exp_f32_e32 v26, v9
	v_mul_f32_e32 v70, v64, v10
	v_mul_f32_e32 v71, v28, v10
	v_mul_f32_e32 v10, v80, v27
	v_mul_f32_e32 v9, 0x3fb8aa3b, v11
	v_mul_f32_e32 v15, 0xbfb8aa3b, v11
	v_mul_f32_e32 v10, 0x3fb8aa3b, v10
	v_exp_f32_e32 v8, v8
	v_exp_f32_e32 v14, v14
	v_exp_f32_e32 v9, v9
	v_exp_f32_e32 v15, v15
	v_exp_f32_e32 v27, v10
	v_sub_f32_e32 v10, v7, v11
	v_mul_f32_e32 v10, 0x3fb8aa3b, v10
	v_exp_f32_e32 v83, v10
	v_pk_mul_f32 v[50:51], v[26:27], v[50:51] neg_lo:[0,1] neg_hi:[0,1]
	v_pk_mul_f32 v[10:11], v[36:37], v[8:9]
	v_pk_mul_f32 v[26:27], v[64:65], v[14:15]
	v_pk_mul_f32 v[14:15], v[28:29], v[14:15]
	v_mul_f32_e32 v8, 0x3fb8aa3b, v20
	v_mul_f32_e32 v28, 0xbfb8aa3b, v20
	s_waitcnt lgkmcnt(0)
; __device__ __forceinline__ unsigned pk2(float lo, float hi) { const f32x2h v = {lo, hi}; const bf16x2h b = __builtin_convertvector(v, bf16x2h); return __builtin_bit_cast(unsigned, b); }
; __device__ __forceinline__ bf16 f2bf(float f) { return (bf16)(pk2(f, f) & 0xffffu); }
; #define CK_BAR() do { asm volatile("s_waitcnt lgkmcnt(0)" ::: "memory"); __builtin_amdgcn_s_barrier(); asm volatile("" ::: "memory"); } while (0)
; __device__ __forceinline__ void phase1(const int WID_, const In& I, char* lds) {
;     ...
;                 ab[e] = -kk_[e] * egm; rb[e] = r_[e] * eg; bb[e] = b_[e] * eng; kb[e] = kp_[e] * eng; bt[e] = b_[e] * egl; kt[e] = kp_[e] * egl; }
; #pragma unroll
;             for (int q = 0; q < 4; ++q) { pab[q] = pk2(ab[2 * q], ab[2 * q + 1]); prb[q] = pk2(rb[2 * q], rb[2 * q + 1]); pbb[q] = pk2(bb[2 * q], bb[2 * q + 1]); pkb[q] = pk2(kb[2 * q], kb[2 * q + 1]); }
;             *(uint4*)(MAT(O_AB) + s * LD + cg * 8) = make_uint4(pab[0], pab[1], pab[2], pab[3]);
;             *(uint4*)(MAT(O_RB) + s * LD + cg * 8) = make_uint4(prb[0], prb[1], prb[2], prb[3]);
;             *(uint4*)(MAT(O_BB) + s * LD + cg * 8) = make_uint4(pbb[0], pbb[1], pbb[2], pbb[3]);
;             *(uint4*)(MAT(O_KB) + s * LD + cg * 8) = make_uint4(pkb[0], pkb[1], pkb[2], pkb[3]);
; #pragma unroll
;             for (int e = 0; e < 8; ++e) { const int k = cg * 8 + e;
;                 MAT(O_AT)[k * LD + s] = f2bf(ab[e]); MAT(O_BT)[k * LD + s] = f2bf(bt[e]); MAT(O_KT)[k * LD + s] = f2bf(kt[e]); MAT(O_VT)[k * LD + s] = f2bf(v_[e]); }
;         }
;         CK_BAR();
	v_sub_f32_e32 v20, v0, v20
	v_mul_f32_e32 v20, 0x3fb8aa3b, v20
	v_exp_f32_e32 v20, v20
	v_pk_mul_f32 v[46:47], v[66:67], v[46:47]
	v_mul_f32_e32 v64, v65, v83
	v_mul_f32_e32 v65, v29, v83
	v_mul_f32_e32 v83, v46, v20
	v_mul_f32_e32 v84, v40, v20
	v_mul_f32_e32 v20, v80, v43
	v_mul_f32_e32 v9, v80, v42
	v_mul_f32_e32 v20, 0x3fb8aa3b, v20
	v_mul_f32_e32 v9, 0x3fb8aa3b, v9
	v_exp_f32_e32 v37, v20
	v_sub_f32_e32 v20, v1, v21
	v_exp_f32_e32 v36, v9
	v_mul_f32_e32 v9, 0x3fb8aa3b, v21
	v_mul_f32_e32 v29, 0xbfb8aa3b, v21
	v_mul_f32_e32 v20, 0x3fb8aa3b, v20
	v_sub_f32_e32 v21, v2, v22
	v_exp_f32_e32 v8, v8
	v_exp_f32_e32 v9, v9
	v_exp_f32_e32 v20, v20
	v_mul_f32_e32 v21, 0x3fb8aa3b, v21
	v_exp_f32_e32 v21, v21
	v_exp_f32_e32 v28, v28
	v_exp_f32_e32 v29, v29
	v_pk_mul_f32 v[34:35], v[48:49], v[34:35]
	v_pk_mul_f32 v[36:37], v[36:37], v[66:67] neg_lo:[0,1] neg_hi:[0,1]
	v_pk_mul_f32 v[32:33], v[32:33], v[8:9]
	v_mul_f32_e32 v66, v47, v20
	v_mul_f32_e32 v67, v41, v20
	v_mul_f32_e32 v9, v80, v44
	v_mul_f32_e32 v8, 0x3fb8aa3b, v22
	v_mul_f32_e32 v20, 0xbfb8aa3b, v22
	v_mul_f32_e32 v22, v80, v45
	v_mul_f32_e32 v9, 0x3fb8aa3b, v9
	v_mul_f32_e32 v85, v34, v21
	v_mul_f32_e32 v86, v30, v21
	v_mul_f32_e32 v21, 0xbfb8aa3b, v23
	v_mul_f32_e32 v22, 0x3fb8aa3b, v22
	v_pk_mul_f32 v[42:43], v[46:47], v[28:29]
	v_pk_mul_f32 v[28:29], v[40:41], v[28:29]
	v_exp_f32_e32 v20, v20
	v_exp_f32_e32 v40, v9
	v_mul_f32_e32 v9, 0x3fb8aa3b, v23
	v_exp_f32_e32 v21, v21
	v_exp_f32_e32 v41, v22
	v_sub_f32_e32 v22, v3, v23
	v_exp_f32_e32 v8, v8
	v_exp_f32_e32 v9, v9
	v_mul_f32_e32 v22, 0x3fb8aa3b, v22
	v_exp_f32_e32 v22, v22
	v_pk_mul_f32 v[40:41], v[40:41], v[48:49] neg_lo:[0,1] neg_hi:[0,1]
	v_pk_mul_f32 v[44:45], v[34:35], v[20:21]
	v_pk_mul_f32 v[46:47], v[30:31], v[20:21]
	v_cvt_pk_bf16_f32 v21, v26, v27
	v_cvt_pk_bf16_f32 v26, v28, v29
	v_mul_lo_u32 v28, v60, s9
	v_lshlrev_b32_e32 v29, 1, v52
	v_pk_mul_f32 v[38:39], v[38:39], v[8:9]
	v_cvt_pk_bf16_f32 v8, v54, v55
	v_cvt_pk_bf16_f32 v12, v12, v13
	v_cvt_pk_bf16_f32 v9, v50, v51
	v_cvt_pk_bf16_f32 v13, v10, v11
	v_cvt_pk_bf16_f32 v10, v36, v37
	v_cvt_pk_bf16_f32 v11, v40, v41
	v_add3_u32 v28, 0, v28, v29
	v_mul_f32_e32 v30, v35, v22
	v_mul_f32_e32 v31, v31, v22
	v_cvt_pk_bf16_f32 v20, v24, v25
	v_cvt_pk_bf16_f32 v24, v62, v63
	v_cvt_pk_bf16_f32 v25, v14, v15
	v_cvt_pk_bf16_f32 v14, v32, v33
	v_cvt_pk_bf16_f32 v22, v42, v43
	v_cvt_pk_bf16_f32 v15, v38, v39
	v_cvt_pk_bf16_f32 v23, v44, v45
	v_cvt_pk_bf16_f32 v27, v46, v47
	ds_write_b128 v28, v[8:11]
	ds_write_b128 v28, v[12:15] offset:9216
	ds_write_b128 v28, v[20:23] offset:18432
	ds_write_b128 v28, v[24:27] offset:27648
	v_and_b32_e32 v35, 2, v61
	v_cmp_ne_u32_e64 s[98:99], 0, v35
	v_bfe_i32 v35, v61, 0, 1
	v_bfe_i32 v38, v60, 0, 1
	v_and_b32_e32 v35, 0x2020202, v35
	v_and_b32_e32 v38, 0x6060606, v38
	v_xor_b32_e32 v32, 0x5040100, v35
	v_xor_b32_e32 v32, v32, v38
	v_and_b32_e32 v33, 3, v61
	v_xor_b32_e32 v33, v60, v33
	v_and_b32_e32 v33, 7, v33
	v_lshl_add_u32 v33, v61, 3, v33
	v_mul_u32_u24_e32 v33, 0x90, v33
	v_and_b32_e32 v34, -8, v60
	v_lshl_add_u32 v33, v34, 1, v33
	v_add_u32_e32 v34, 0x12000, v33
	v_cvt_pk_bf16_f32 v81, v81, v56
	v_cvt_pk_bf16_f32 v70, v70, v64
	v_cvt_pk_bf16_f32 v83, v83, v66
	v_cvt_pk_bf16_f32 v85, v85, v30
	v_cvt_pk_bf16_f32 v82, v82, v57
	v_cvt_pk_bf16_f32 v71, v71, v65
	v_cvt_pk_bf16_f32 v84, v84, v67
	v_cvt_pk_bf16_f32 v86, v86, v31
	v_cvt_pk_bf16_f32 v53, v53, v68
	v_cvt_pk_bf16_f32 v72, v72, v73
	v_cvt_pk_bf16_f32 v74, v74, v75
	v_cvt_pk_bf16_f32 v78, v78, v79
	v_mov_b32_dpp v55, v8 row_ror:8 row_mask:0xf bank_mask:0xf
	v_mov_b32_dpp v51, v9 row_ror:8 row_mask:0xf bank_mask:0xf
	v_mov_b32_dpp v37, v10 row_ror:8 row_mask:0xf bank_mask:0xf
	v_mov_b32_dpp v41, v11 row_ror:8 row_mask:0xf bank_mask:0xf
	v_mov_b32_dpp v56, v81 row_ror:8 row_mask:0xf bank_mask:0xf
	v_mov_b32_dpp v64, v70 row_ror:8 row_mask:0xf bank_mask:0xf
	v_mov_b32_dpp v66, v83 row_ror:8 row_mask:0xf bank_mask:0xf
	v_mov_b32_dpp v30, v85 row_ror:8 row_mask:0xf bank_mask:0xf
	v_mov_b32_dpp v57, v82 row_ror:8 row_mask:0xf bank_mask:0xf
	v_mov_b32_dpp v65, v71 row_ror:8 row_mask:0xf bank_mask:0xf
	v_mov_b32_dpp v67, v84 row_ror:8 row_mask:0xf bank_mask:0xf
	v_mov_b32_dpp v31, v86 row_ror:8 row_mask:0xf bank_mask:0xf
	v_mov_b32_dpp v68, v53 row_ror:8 row_mask:0xf bank_mask:0xf
	v_mov_b32_dpp v73, v72 row_ror:8 row_mask:0xf bank_mask:0xf
	v_mov_b32_dpp v75, v74 row_ror:8 row_mask:0xf bank_mask:0xf
	v_mov_b32_dpp v79, v78 row_ror:8 row_mask:0xf bank_mask:0xf
	v_perm_b32 v54, v55, v8, v32
	v_perm_b32 v50, v51, v9, v32
	v_perm_b32 v36, v37, v10, v32
	v_perm_b32 v40, v41, v11, v32
	v_perm_b32 v81, v56, v81, v32
	v_perm_b32 v70, v64, v70, v32
	v_perm_b32 v83, v66, v83, v32
	v_perm_b32 v85, v30, v85, v32
	v_perm_b32 v82, v57, v82, v32
	v_perm_b32 v71, v65, v71, v32
	v_perm_b32 v84, v67, v84, v32
	v_perm_b32 v86, v31, v86, v32
	v_perm_b32 v53, v68, v53, v32
	v_perm_b32 v72, v73, v72, v32
	v_perm_b32 v74, v75, v74, v32
	v_perm_b32 v78, v79, v78, v32
	v_cndmask_b32_e64 v8, v54, v50, s[98:99]
	v_cndmask_b32_e64 v9, v50, v54, s[98:99]
	v_cndmask_b32_e64 v10, v36, v40, s[98:99]
	v_cndmask_b32_e64 v11, v40, v36, s[98:99]
	v_cndmask_b32_e64 v12, v81, v70, s[98:99]
	v_cndmask_b32_e64 v13, v70, v81, s[98:99]
	v_cndmask_b32_e64 v14, v83, v85, s[98:99]
	v_cndmask_b32_e64 v15, v85, v83, s[98:99]
	v_cndmask_b32_e64 v20, v82, v71, s[98:99]
	v_cndmask_b32_e64 v21, v71, v82, s[98:99]
	v_cndmask_b32_e64 v22, v84, v86, s[98:99]
	v_cndmask_b32_e64 v23, v86, v84, s[98:99]
	v_cndmask_b32_e64 v24, v53, v72, s[98:99]
	v_cndmask_b32_e64 v25, v72, v53, s[98:99]
	v_cndmask_b32_e64 v26, v74, v78, s[98:99]
	v_cndmask_b32_e64 v27, v78, v74, s[98:99]
	v_permlane16_swap_b32_e32 v8, v9
	v_permlane16_swap_b32_e32 v10, v11
	v_permlane16_swap_b32_e32 v12, v13
	v_permlane16_swap_b32_e32 v14, v15
	v_permlane16_swap_b32_e32 v20, v21
	v_permlane16_swap_b32_e32 v22, v23
	v_permlane16_swap_b32_e32 v24, v25
	v_permlane16_swap_b32_e32 v26, v27
	v_permlane32_swap_b32_e32 v8, v10
	v_permlane32_swap_b32_e32 v9, v11
	v_permlane32_swap_b32_e32 v12, v14
	v_permlane32_swap_b32_e32 v13, v15
	v_permlane32_swap_b32_e32 v20, v22
	v_permlane32_swap_b32_e32 v21, v23
	v_permlane32_swap_b32_e32 v24, v26
	v_permlane32_swap_b32_e32 v25, v27
	s_nop 1
	ds_write_b128 v33, v[8:11] offset:36864
	ds_write_b128 v33, v[12:15] offset:55296
	ds_write_b128 v33, v[20:23] offset:64512
	ds_write_b128 v34, v[24:27]
	s_waitcnt lgkmcnt(0)
	s_barrier
; __device__ __forceinline__ void phase1(const int WID_, const In& I, char* lds) {
;     ...
;         P1_LOADS(item + GN);
;         if (s == 63) {
; #pragma unroll
;             for (int e = 0; e < 8; ++e) TOT[cg * 8 + e] = __expf(glast[e]);
;         }
	v_mbcnt_lo_u32_b32 v8, -1, 0
	v_mbcnt_hi_u32_b32 v8, -1, v8
	s_ashr_i32 s0, s1, 10
	v_add_u32_e32 v9, s86, v8
	s_lshr_b32 s4, s1, 1
	s_lshl_b32 s1, s1, 6
	v_ashrrev_i32_e32 v9, 3, v9
	s_and_b32 s4, s4, 0x1c0
	v_lshlrev_b32_e32 v8, 3, v8
	s_and_b32 s1, s1, 0x1fc0
	v_and_or_b32 v14, v8, 56, s4
	v_add_u32_e32 v8, s1, v9
	s_ashr_i32 s1, s0, 31
	s_lshl_b64 s[0:1], s[0:1], 13
	v_ashrrev_i32_e32 v9, 31, v8
	v_lshl_add_u64 v[10:11], s[0:1], 0, v[8:9]
	v_mov_b64_e32 v[12:13], s[92:93]
	v_mad_u64_u32 v[12:13], s[0:1], v10, s8, v[12:13]
	v_mad_i32_i24 v13, v11, s8, v13
	v_lshlrev_b32_e32 v68, 1, v14
	v_cmp_lt_i32_e32 vcc, 0, v8
	v_lshl_add_u64 v[12:13], v[12:13], 0, v[68:69]
	v_readlane_b32 s0, v242, 37
	v_cndmask_b32_e64 v9, 0, -1, vcc
	v_cndmask_b32_e32 v8, 0, v76, vcc
	v_lshl_add_u64 v[8:9], v[12:13], 0, v[8:9]
	global_load_dwordx4 v[36:39], v[12:13], off nt
	global_load_dwordx4 v[28:31], v[12:13], off offset:1024 nt
	global_load_dwordx4 v[20:23], v[12:13], off offset:2048 nt
	global_load_dwordx4 v[44:47], v[8:9], off nt
	global_load_dwordx4 v[48:51], v[8:9], off offset:1024 nt
	global_load_dwordx4 v[24:27], v[8:9], off offset:2048 nt
	v_lshlrev_b64 v[8:9], 10, v[10:11]
	v_readlane_b32 s1, v242, 38
	v_cmp_eq_u32_e32 vcc, 63, v60
	s_nop 0
	v_lshl_add_u64 v[10:11], s[0:1], 0, v[8:9]
	v_lshl_add_u64 v[10:11], v[10:11], 0, v[68:69]
	v_lshl_add_u64 v[8:9], s[28:29], 0, v[8:9]
	v_lshl_add_u64 v[8:9], v[8:9], 0, v[68:69]
	global_load_dwordx4 v[32:35], v[10:11], off nt
	global_load_dwordx4 v[40:43], v[8:9], off nt
	s_and_saveexec_b64 s[0:1], vcc
	s_cbranch_execz .LBB0_1428
	v_mul_f32_e32 v4, 0x3fb8aa3b, v4
	v_mul_f32_e32 v5, 0x3fb8aa3b, v5
	v_mul_f32_e32 v6, 0x3fb8aa3b, v6
	v_mul_f32_e32 v7, 0x3fb8aa3b, v7
	v_exp_f32_e32 v4, v4
	v_exp_f32_e32 v5, v5
	v_exp_f32_e32 v6, v6
	v_exp_f32_e32 v7, v7
	v_mul_f32_e32 v0, 0x3fb8aa3b, v0
	v_mul_f32_e32 v1, 0x3fb8aa3b, v1
	v_mul_f32_e32 v2, 0x3fb8aa3b, v2
	v_mul_f32_e32 v3, 0x3fb8aa3b, v3
	v_exp_f32_e32 v0, v0
	v_exp_f32_e32 v1, v1
	v_exp_f32_e32 v2, v2
	v_exp_f32_e32 v3, v3
	v_lshl_add_u32 v8, v52, 2, 0
	v_add_u32_e32 v8, 0x21400, v8
	ds_write_b128 v8, v[4:7]
	ds_write_b128 v8, v[0:3] offset:16
